# FF2 K loop: LDS-DMA in scalar-base + 32-bit lane offset form (no VALU address adds), ds_read base hoisted; on top of v045
# speedup vs baseline: 1.0021x; 1.0004x over previous
.LBB0_1951:
	v_mov_b32_e32 v177, 0
	s_andn2_b64 vcc, exec, s[58:59]
	v_mov_b32_e32 v176, v177
	v_mov_b32_e32 v175, v177
	v_mov_b32_e32 v174, v177
	v_mov_b32_e32 v181, v177
	v_mov_b32_e32 v180, v177
	v_mov_b32_e32 v179, v177
	v_mov_b32_e32 v178, v177
	v_mov_b32_e32 v157, v177
	v_mov_b32_e32 v156, v177
	v_mov_b32_e32 v155, v177
	v_mov_b32_e32 v154, v177
	v_mov_b32_e32 v153, v177
	v_mov_b32_e32 v152, v177
	v_mov_b32_e32 v151, v177
	v_mov_b32_e32 v150, v177
	v_mov_b32_e32 v133, v177
	v_mov_b32_e32 v132, v177
	v_mov_b32_e32 v131, v177
	v_mov_b32_e32 v130, v177
	v_mov_b32_e32 v129, v177
	v_mov_b32_e32 v128, v177
	v_mov_b32_e32 v127, v177
	v_mov_b32_e32 v126, v177
	v_mov_b32_e32 v113, v177
	v_mov_b32_e32 v112, v177
	v_mov_b32_e32 v111, v177
	v_mov_b32_e32 v110, v177
	v_mov_b32_e32 v109, v177
	v_mov_b32_e32 v108, v177
	v_mov_b32_e32 v107, v177
	v_mov_b32_e32 v106, v177
	v_mov_b32_e32 v169, v177
	v_mov_b32_e32 v168, v177
	v_mov_b32_e32 v167, v177
	v_mov_b32_e32 v166, v177
	v_mov_b32_e32 v165, v177
	v_mov_b32_e32 v164, v177
	v_mov_b32_e32 v163, v177
	v_mov_b32_e32 v162, v177
	v_mov_b32_e32 v145, v177
	v_mov_b32_e32 v144, v177
	v_mov_b32_e32 v143, v177
	v_mov_b32_e32 v142, v177
	v_mov_b32_e32 v141, v177
	v_mov_b32_e32 v140, v177
	v_mov_b32_e32 v139, v177
	v_mov_b32_e32 v138, v177
	v_mov_b32_e32 v121, v177
	v_mov_b32_e32 v120, v177
	v_mov_b32_e32 v119, v177
	v_mov_b32_e32 v118, v177
	v_mov_b32_e32 v117, v177
	v_mov_b32_e32 v116, v177
	v_mov_b32_e32 v115, v177
	v_mov_b32_e32 v114, v177
	v_mov_b32_e32 v105, v177
	v_mov_b32_e32 v104, v177
	v_mov_b32_e32 v103, v177
	v_mov_b32_e32 v102, v177
	v_mov_b32_e32 v101, v177
	v_mov_b32_e32 v100, v177
	v_mov_b32_e32 v99, v177
	v_mov_b32_e32 v98, v177
	v_mov_b32_e32 v97, v177
	v_mov_b32_e32 v96, v177
	v_mov_b32_e32 v95, v177
	v_mov_b32_e32 v94, v177
	v_mov_b32_e32 v93, v177
	v_mov_b32_e32 v92, v177
	v_mov_b32_e32 v91, v177
	v_mov_b32_e32 v90, v177
	v_mov_b32_e32 v81, v177
	v_mov_b32_e32 v80, v177
	v_mov_b32_e32 v79, v177
	v_mov_b32_e32 v78, v177
	v_mov_b32_e32 v77, v177
	v_mov_b32_e32 v76, v177
	v_mov_b32_e32 v75, v177
	v_mov_b32_e32 v74, v177
	v_mov_b32_e32 v57, v177
	v_mov_b32_e32 v56, v177
	v_mov_b32_e32 v55, v177
	v_mov_b32_e32 v54, v177
	v_mov_b32_e32 v53, v177
	v_mov_b32_e32 v52, v177
	v_mov_b32_e32 v51, v177
	v_mov_b32_e32 v50, v177
	v_mov_b32_e32 v17, v177
	v_mov_b32_e32 v16, v177
	v_mov_b32_e32 v15, v177
	v_mov_b32_e32 v14, v177
	v_mov_b32_e32 v13, v177
	v_mov_b32_e32 v12, v177
	v_mov_b32_e32 v11, v177
	v_mov_b32_e32 v10, v177
	v_mov_b32_e32 v89, v177
	v_mov_b32_e32 v88, v177
	v_mov_b32_e32 v87, v177
	v_mov_b32_e32 v86, v177
	v_mov_b32_e32 v85, v177
	v_mov_b32_e32 v84, v177
	v_mov_b32_e32 v83, v177
	v_mov_b32_e32 v82, v177
	v_mov_b32_e32 v73, v177
	v_mov_b32_e32 v72, v177
	v_mov_b32_e32 v71, v177
	v_mov_b32_e32 v70, v177
	v_mov_b32_e32 v69, v177
	v_mov_b32_e32 v68, v177
	v_mov_b32_e32 v67, v177
	v_mov_b32_e32 v66, v177
	v_mov_b32_e32 v41, v177
	v_mov_b32_e32 v40, v177
	v_mov_b32_e32 v39, v177
	v_mov_b32_e32 v38, v177
	v_mov_b32_e32 v37, v177
	v_mov_b32_e32 v36, v177
	v_mov_b32_e32 v35, v177
	v_mov_b32_e32 v34, v177
	v_mov_b32_e32 v9, v177
	v_mov_b32_e32 v8, v177
	v_mov_b32_e32 v7, v177
	v_mov_b32_e32 v6, v177
	s_waitcnt lgkmcnt(0)
	v_mov_b32_e32 v5, v177
	v_mov_b32_e32 v4, v177
	v_mov_b32_e32 v3, v177
	v_mov_b32_e32 v2, v177
	s_cbranch_vccnz .LBB0_1954
	s_add_u32 s38, s42, 0x80
	s_addc_u32 s39, s43, 0
	s_add_u32 s42, s40, 0x100
	v_mov_b32_e32 v2, 0
	s_addc_u32 s43, s41, 0
	s_mov_b32 s40, 0
	v_mov_b32_e32 v3, v2
	v_mov_b32_e32 v4, v2
	v_mov_b32_e32 v5, v2
	v_mov_b32_e32 v6, v2
	v_mov_b32_e32 v7, v2
	v_mov_b32_e32 v8, v2
	v_mov_b32_e32 v9, v2
	v_mov_b32_e32 v34, v2
	v_mov_b32_e32 v35, v2
	v_mov_b32_e32 v36, v2
	v_mov_b32_e32 v37, v2
	v_mov_b32_e32 v38, v2
	v_mov_b32_e32 v39, v2
	v_mov_b32_e32 v40, v2
	v_mov_b32_e32 v41, v2
	v_mov_b32_e32 v66, v2
	v_mov_b32_e32 v67, v2
	v_mov_b32_e32 v68, v2
	v_mov_b32_e32 v69, v2
	v_mov_b32_e32 v70, v2
	v_mov_b32_e32 v71, v2
	v_mov_b32_e32 v72, v2
	v_mov_b32_e32 v73, v2
	v_mov_b32_e32 v82, v2
	v_mov_b32_e32 v83, v2
	v_mov_b32_e32 v84, v2
	v_mov_b32_e32 v85, v2
	v_mov_b32_e32 v86, v2
	v_mov_b32_e32 v87, v2
	v_mov_b32_e32 v88, v2
	v_mov_b32_e32 v89, v2
	v_mov_b32_e32 v10, v2
	v_mov_b32_e32 v11, v2
	v_mov_b32_e32 v12, v2
	v_mov_b32_e32 v13, v2
	v_mov_b32_e32 v14, v2
	v_mov_b32_e32 v15, v2
	v_mov_b32_e32 v16, v2
	v_mov_b32_e32 v17, v2
	v_mov_b32_e32 v50, v2
	v_mov_b32_e32 v51, v2
	v_mov_b32_e32 v52, v2
	v_mov_b32_e32 v53, v2
	v_mov_b32_e32 v54, v2
	v_mov_b32_e32 v55, v2
	v_mov_b32_e32 v56, v2
	v_mov_b32_e32 v57, v2
	v_mov_b32_e32 v74, v2
	v_mov_b32_e32 v75, v2
	v_mov_b32_e32 v76, v2
	v_mov_b32_e32 v77, v2
	v_mov_b32_e32 v78, v2
	v_mov_b32_e32 v79, v2
	v_mov_b32_e32 v80, v2
	v_mov_b32_e32 v81, v2
	v_mov_b32_e32 v90, v2
	v_mov_b32_e32 v91, v2
	v_mov_b32_e32 v92, v2
	v_mov_b32_e32 v93, v2
	v_mov_b32_e32 v94, v2
	v_mov_b32_e32 v95, v2
	v_mov_b32_e32 v96, v2
	v_mov_b32_e32 v97, v2
	v_mov_b32_e32 v98, v2
	v_mov_b32_e32 v99, v2
	v_mov_b32_e32 v100, v2
	v_mov_b32_e32 v101, v2
	v_mov_b32_e32 v102, v2
	v_mov_b32_e32 v103, v2
	v_mov_b32_e32 v104, v2
	v_mov_b32_e32 v105, v2
	v_mov_b32_e32 v114, v2
	v_mov_b32_e32 v115, v2
	v_mov_b32_e32 v116, v2
	v_mov_b32_e32 v117, v2
	v_mov_b32_e32 v118, v2
	v_mov_b32_e32 v119, v2
	v_mov_b32_e32 v120, v2
	v_mov_b32_e32 v121, v2
	v_mov_b32_e32 v138, v2
	v_mov_b32_e32 v139, v2
	v_mov_b32_e32 v140, v2
	v_mov_b32_e32 v141, v2
	v_mov_b32_e32 v142, v2
	v_mov_b32_e32 v143, v2
	v_mov_b32_e32 v144, v2
	v_mov_b32_e32 v145, v2
	v_mov_b32_e32 v162, v2
	v_mov_b32_e32 v163, v2
	v_mov_b32_e32 v164, v2
	v_mov_b32_e32 v165, v2
	v_mov_b32_e32 v166, v2
	v_mov_b32_e32 v167, v2
	v_mov_b32_e32 v168, v2
	v_mov_b32_e32 v169, v2
	v_mov_b32_e32 v106, v2
	v_mov_b32_e32 v107, v2
	v_mov_b32_e32 v108, v2
	v_mov_b32_e32 v109, v2
	v_mov_b32_e32 v110, v2
	v_mov_b32_e32 v111, v2
	v_mov_b32_e32 v112, v2
	v_mov_b32_e32 v113, v2
	v_mov_b32_e32 v126, v2
	v_mov_b32_e32 v127, v2
	v_mov_b32_e32 v128, v2
	v_mov_b32_e32 v129, v2
	v_mov_b32_e32 v130, v2
	v_mov_b32_e32 v131, v2
	v_mov_b32_e32 v132, v2
	v_mov_b32_e32 v133, v2
	v_mov_b32_e32 v150, v2
	v_mov_b32_e32 v151, v2
	v_mov_b32_e32 v152, v2
	v_mov_b32_e32 v153, v2
	v_mov_b32_e32 v154, v2
	v_mov_b32_e32 v155, v2
	v_mov_b32_e32 v156, v2
	v_mov_b32_e32 v157, v2
	v_mov_b32_e32 v178, v2
	v_mov_b32_e32 v179, v2
	v_mov_b32_e32 v180, v2
	v_mov_b32_e32 v181, v2
	v_mov_b32_e32 v174, v2
	v_mov_b32_e32 v175, v2
	v_mov_b32_e32 v176, v2
	v_mov_b32_e32 v177, v2
	v_add_u32_e32 v235, 0x10000, v247
.LBB0_1953:
	s_add_i32 s44, s40, 2
	s_add_u32 s7, s38, 0x80
	s_addc_u32 s10, s39, 0
	s_add_i32 s45, 0, 0x10000
	s_cmp_eq_u32 s74, s40
	s_cselect_b32 s41, s65, s10
	s_cselect_b32 s40, s64, s7
	s_cselect_b32 s11, s67, s43
	s_cselect_b32 s10, s66, s42
	s_add_i32 s7, 0, 0x14000
	ds_read_b128 v[18:21], v235
	ds_read_b128 v[22:25], v235 offset:1024
	ds_read_b128 v[26:29], v235 offset:2048
	ds_read_b128 v[30:33], v235 offset:3072
	ds_read_b128 v[42:45], v235 offset:16384
	ds_read_b128 v[46:49], v235 offset:17408
	ds_read_b128 v[58:61], v235 offset:18432
	ds_read_b128 v[62:65], v235 offset:19456
	s_add_i32 m0, s17, 0xc000
	ds_read_b128 v[122:125], v248
	ds_read_b128 v[134:137], v248 offset:1024
	ds_read_b128 v[146:149], v248 offset:2048
	ds_read_b128 v[158:161], v248 offset:3072
	ds_read_b128 v[170:173], v248 offset:4096
	ds_read_b128 v[182:185], v248 offset:5120
	ds_read_b128 v[186:189], v248 offset:6144
	ds_read_b128 v[210:213], v248 offset:7168
	global_load_lds_dwordx4 v198, s[38:39]
	s_add_i32 m0, s17, 0xe000
	s_nop 0
	global_load_lds_dwordx4 v200, s[38:39]
	s_waitcnt vmcnt(8)
	s_waitcnt lgkmcnt(0)
	s_setprio 1
	s_barrier
	s_setprio 1
	s_waitcnt lgkmcnt(0)
	v_mfma_f32_16x16x32_bf16 v[174:177], v[18:21], v[122:125], v[174:177]
	v_mfma_f32_16x16x32_bf16 v[178:181], v[26:29], v[122:125], v[178:181]
	v_mfma_f32_16x16x32_bf16 v[154:157], v[18:21], v[146:149], v[154:157]
	v_mfma_f32_16x16x32_bf16 v[150:153], v[26:29], v[146:149], v[150:153]
	v_mfma_f32_16x16x32_bf16 v[130:133], v[18:21], v[170:173], v[130:133]
	v_mfma_f32_16x16x32_bf16 v[126:129], v[26:29], v[170:173], v[126:129]
	v_mfma_f32_16x16x32_bf16 v[110:113], v[18:21], v[186:189], v[110:113]
	v_mfma_f32_16x16x32_bf16 v[106:109], v[26:29], v[186:189], v[106:109]
	v_mfma_f32_16x16x32_bf16 v[174:177], v[22:25], v[134:137], v[174:177]
	v_mfma_f32_16x16x32_bf16 v[178:181], v[30:33], v[134:137], v[178:181]
	v_mfma_f32_16x16x32_bf16 v[154:157], v[22:25], v[158:161], v[154:157]
	v_mfma_f32_16x16x32_bf16 v[150:153], v[30:33], v[158:161], v[150:153]
	v_mfma_f32_16x16x32_bf16 v[130:133], v[22:25], v[182:185], v[130:133]
	v_mfma_f32_16x16x32_bf16 v[126:129], v[30:33], v[182:185], v[126:129]
	v_mfma_f32_16x16x32_bf16 v[110:113], v[22:25], v[210:213], v[110:113]
	v_mfma_f32_16x16x32_bf16 v[106:109], v[30:33], v[210:213], v[106:109]
	s_setprio 0
	s_setprio 1
	v_mfma_f32_16x16x32_bf16 v[166:169], v[42:45], v[122:125], v[166:169]
	v_mfma_f32_16x16x32_bf16 v[122:125], v[58:61], v[122:125], v[162:165]
	v_mfma_f32_16x16x32_bf16 v[138:141], v[58:61], v[146:149], v[138:141]
	v_mfma_f32_16x16x32_bf16 v[118:121], v[42:45], v[170:173], v[118:121]
	v_mfma_f32_16x16x32_bf16 v[114:117], v[58:61], v[170:173], v[114:117]
	v_mfma_f32_16x16x32_bf16 v[102:105], v[42:45], v[186:189], v[102:105]
	v_mfma_f32_16x16x32_bf16 v[98:101], v[58:61], v[186:189], v[98:101]
	v_mfma_f32_16x16x32_bf16 v[166:169], v[46:49], v[134:137], v[166:169]
	v_mfma_f32_16x16x32_bf16 v[122:125], v[62:65], v[134:137], v[122:125]
	v_mfma_f32_16x16x32_bf16 v[134:137], v[42:45], v[146:149], v[142:145]
	v_mfma_f32_16x16x32_bf16 v[138:141], v[62:65], v[158:161], v[138:141]
	v_mfma_f32_16x16x32_bf16 v[118:121], v[46:49], v[182:185], v[118:121]
	v_mfma_f32_16x16x32_bf16 v[114:117], v[62:65], v[182:185], v[114:117]
	v_mfma_f32_16x16x32_bf16 v[102:105], v[46:49], v[210:213], v[102:105]
	v_mfma_f32_16x16x32_bf16 v[98:101], v[62:65], v[210:213], v[98:101]
	v_mfma_f32_16x16x32_bf16 v[134:137], v[46:49], v[158:161], v[134:137]
	s_setprio 0
	s_barrier
	s_add_i32 s45, s45, s16
	s_mov_b32 m0, s45
	ds_read_b128 v[142:145], v248 offset:16384
	ds_read_b128 v[146:149], v248 offset:17408
	ds_read_b128 v[158:161], v248 offset:18432
	ds_read_b128 v[162:165], v248 offset:19456
	ds_read_b128 v[170:173], v248 offset:20480
	ds_read_b128 v[182:185], v248 offset:21504
	ds_read_b128 v[186:189], v248 offset:22528
	ds_read_b128 v[210:213], v248 offset:23552
	global_load_lds_dwordx4 v192, s[10:11]
	s_add_i32 m0, s45, 0x2000
	s_add_i32 s7, s7, s16
	global_load_lds_dwordx4 v196, s[10:11]
	s_add_u32 s10, s10, s0
	s_addc_u32 s11, s11, s1
	s_mov_b32 m0, s7
	s_nop 0
	global_load_lds_dwordx4 v192, s[10:11]
	s_add_i32 m0, s7, 0x2000
	s_nop 0
	global_load_lds_dwordx4 v196, s[10:11]
	s_mov_b32 m0, s17
	s_nop 0
	global_load_lds_dwordx4 v190, s[40:41]
	s_mov_b32 m0, s23
	s_nop 0
	global_load_lds_dwordx4 v194, s[40:41]
	s_waitcnt vmcnt(8)
	s_waitcnt lgkmcnt(0)
	s_setprio 1
	s_barrier
	s_setprio 1
	s_waitcnt lgkmcnt(0)
	v_mfma_f32_16x16x32_bf16 v[94:97], v[18:21], v[142:145], v[94:97]
	v_mfma_f32_16x16x32_bf16 v[90:93], v[26:29], v[142:145], v[90:93]
	v_mfma_f32_16x16x32_bf16 v[78:81], v[18:21], v[158:161], v[78:81]
	v_mfma_f32_16x16x32_bf16 v[74:77], v[26:29], v[158:161], v[74:77]
	v_mfma_f32_16x16x32_bf16 v[54:57], v[18:21], v[170:173], v[54:57]
	v_mfma_f32_16x16x32_bf16 v[50:53], v[26:29], v[170:173], v[50:53]
	v_mfma_f32_16x16x32_bf16 v[14:17], v[18:21], v[186:189], v[14:17]
	v_mfma_f32_16x16x32_bf16 v[10:13], v[26:29], v[186:189], v[10:13]
	v_mfma_f32_16x16x32_bf16 v[94:97], v[22:25], v[146:149], v[94:97]
	v_mfma_f32_16x16x32_bf16 v[90:93], v[30:33], v[146:149], v[90:93]
	v_mfma_f32_16x16x32_bf16 v[78:81], v[22:25], v[162:165], v[78:81]
	v_mfma_f32_16x16x32_bf16 v[74:77], v[30:33], v[162:165], v[74:77]
	v_mfma_f32_16x16x32_bf16 v[54:57], v[22:25], v[182:185], v[54:57]
	v_mfma_f32_16x16x32_bf16 v[50:53], v[30:33], v[182:185], v[50:53]
	v_mfma_f32_16x16x32_bf16 v[14:17], v[22:25], v[210:213], v[14:17]
	v_mfma_f32_16x16x32_bf16 v[10:13], v[30:33], v[210:213], v[10:13]
	s_setprio 0
	s_setprio 1
	v_mfma_f32_16x16x32_bf16 v[38:41], v[42:45], v[170:173], v[38:41]
	v_mfma_f32_16x16x32_bf16 v[34:37], v[58:61], v[170:173], v[34:37]
	v_mfma_f32_16x16x32_bf16 v[6:9], v[42:45], v[186:189], v[6:9]
	v_mfma_f32_16x16x32_bf16 v[2:5], v[58:61], v[186:189], v[2:5]
	v_mfma_f32_16x16x32_bf16 v[18:21], v[42:45], v[142:145], v[86:89]
	v_mfma_f32_16x16x32_bf16 v[22:25], v[58:61], v[142:145], v[82:85]
	v_mfma_f32_16x16x32_bf16 v[26:29], v[42:45], v[158:161], v[70:73]
	v_mfma_f32_16x16x32_bf16 v[30:33], v[58:61], v[158:161], v[66:69]
	v_mfma_f32_16x16x32_bf16 v[38:41], v[46:49], v[182:185], v[38:41]
	v_mfma_f32_16x16x32_bf16 v[34:37], v[62:65], v[182:185], v[34:37]
	v_mfma_f32_16x16x32_bf16 v[6:9], v[46:49], v[210:213], v[6:9]
	v_mfma_f32_16x16x32_bf16 v[2:5], v[62:65], v[210:213], v[2:5]
	v_mfma_f32_16x16x32_bf16 v[18:21], v[46:49], v[146:149], v[18:21]
	v_mfma_f32_16x16x32_bf16 v[22:25], v[62:65], v[146:149], v[22:25]
	v_mfma_f32_16x16x32_bf16 v[26:29], v[46:49], v[162:165], v[26:29]
	v_mfma_f32_16x16x32_bf16 v[30:33], v[62:65], v[162:165], v[30:33]
	s_setprio 0
	s_barrier
	s_add_i32 s7, 0, 0x18000
	s_add_i32 s45, 0, 0x1c000
	ds_read_b128 v[42:45], v235 offset:32768
	ds_read_b128 v[46:49], v235 offset:33792
	ds_read_b128 v[58:61], v235 offset:34816
	ds_read_b128 v[62:65], v235 offset:35840
	ds_read_b128 v[146:149], v235 offset:49152
	ds_read_b128 v[158:161], v235 offset:50176
	ds_read_b128 v[170:173], v235 offset:51200
	ds_read_b128 v[182:185], v235 offset:52224
	s_add_u32 s10, s40, s0
	s_addc_u32 s11, s41, s1
	s_mov_b32 m0, s68
	ds_read_b128 v[66:69], v248 offset:32768
	ds_read_b128 v[70:73], v248 offset:33792
	ds_read_b128 v[82:85], v248 offset:34816
	ds_read_b128 v[86:89], v248 offset:35840
	ds_read_b128 v[186:189], v248 offset:36864
	ds_read_b128 v[210:213], v248 offset:37888
	ds_read_b128 v[214:217], v248 offset:38912
	ds_read_b128 v[218:221], v248 offset:39936
	global_load_lds_dwordx4 v190, s[10:11]
	s_mov_b32 m0, s69
	s_nop 0
	global_load_lds_dwordx4 v194, s[10:11]
	s_waitcnt vmcnt(8)
	s_waitcnt lgkmcnt(0)
	s_setprio 1
	s_barrier
	s_setprio 1
	s_waitcnt lgkmcnt(0)
	v_mfma_f32_16x16x32_bf16 v[142:145], v[42:45], v[66:69], v[174:177]
	v_mfma_f32_16x16x32_bf16 v[174:177], v[46:49], v[70:73], v[142:145]
	v_mfma_f32_16x16x32_bf16 v[142:145], v[58:61], v[66:69], v[178:181]
	v_mfma_f32_16x16x32_bf16 v[178:181], v[62:65], v[70:73], v[142:145]
	v_mfma_f32_16x16x32_bf16 v[142:145], v[42:45], v[82:85], v[154:157]
	v_mfma_f32_16x16x32_bf16 v[154:157], v[46:49], v[86:89], v[142:145]
	v_mfma_f32_16x16x32_bf16 v[142:145], v[58:61], v[82:85], v[150:153]
	v_mfma_f32_16x16x32_bf16 v[130:133], v[42:45], v[186:189], v[130:133]
	v_mfma_f32_16x16x32_bf16 v[126:129], v[58:61], v[186:189], v[126:129]
	v_mfma_f32_16x16x32_bf16 v[110:113], v[42:45], v[214:217], v[110:113]
	v_mfma_f32_16x16x32_bf16 v[106:109], v[58:61], v[214:217], v[106:109]
	v_mfma_f32_16x16x32_bf16 v[150:153], v[62:65], v[86:89], v[142:145]
	v_mfma_f32_16x16x32_bf16 v[130:133], v[46:49], v[210:213], v[130:133]
	v_mfma_f32_16x16x32_bf16 v[126:129], v[62:65], v[210:213], v[126:129]
	v_mfma_f32_16x16x32_bf16 v[110:113], v[46:49], v[218:221], v[110:113]
	v_mfma_f32_16x16x32_bf16 v[106:109], v[62:65], v[218:221], v[106:109]
	s_setprio 0
	s_setprio 1
	v_mfma_f32_16x16x32_bf16 v[142:145], v[146:149], v[66:69], v[166:169]
	v_mfma_f32_16x16x32_bf16 v[66:69], v[170:173], v[66:69], v[122:125]
	v_mfma_f32_16x16x32_bf16 v[162:165], v[182:185], v[70:73], v[66:69]
	v_mfma_f32_16x16x32_bf16 v[66:69], v[146:149], v[82:85], v[134:137]
	v_mfma_f32_16x16x32_bf16 v[166:169], v[158:161], v[70:73], v[142:145]
	v_mfma_f32_16x16x32_bf16 v[142:145], v[158:161], v[86:89], v[66:69]
	v_mfma_f32_16x16x32_bf16 v[66:69], v[170:173], v[82:85], v[138:141]
	v_mfma_f32_16x16x32_bf16 v[138:141], v[182:185], v[86:89], v[66:69]
	v_mfma_f32_16x16x32_bf16 v[66:69], v[146:149], v[186:189], v[118:121]
	v_mfma_f32_16x16x32_bf16 v[118:121], v[158:161], v[210:213], v[66:69]
	v_mfma_f32_16x16x32_bf16 v[66:69], v[170:173], v[186:189], v[114:117]
	v_mfma_f32_16x16x32_bf16 v[114:117], v[182:185], v[210:213], v[66:69]
	v_mfma_f32_16x16x32_bf16 v[66:69], v[146:149], v[214:217], v[102:105]
	v_mfma_f32_16x16x32_bf16 v[102:105], v[158:161], v[218:221], v[66:69]
	v_mfma_f32_16x16x32_bf16 v[66:69], v[170:173], v[214:217], v[98:101]
	v_mfma_f32_16x16x32_bf16 v[98:101], v[182:185], v[218:221], v[66:69]
	s_setprio 0
	s_barrier
	s_add_i32 s7, s7, s16
	s_mov_b32 m0, s7
	s_add_i32 s98, s74, 2
	s_cmp_eq_u32 s98, s44
	s_cselect_b32 s98, s66, s42
	s_cselect_b32 s99, s67, s43
	s_add_u32 s98, s98, s14
	s_addc_u32 s99, s99, s15
	ds_read_b128 v[66:69], v248 offset:49152
	ds_read_b128 v[70:73], v248 offset:50176
	ds_read_b128 v[122:125], v248 offset:51200
	ds_read_b128 v[134:137], v248 offset:52224
	ds_read_b128 v[186:189], v248 offset:53248
	ds_read_b128 v[210:213], v248 offset:54272
	ds_read_b128 v[214:217], v248 offset:55296
	ds_read_b128 v[218:221], v248 offset:56320
	global_load_lds_dwordx4 v192, s[98:99]
	s_add_i32 m0, s7, 0x2000
	s_add_i32 s7, s45, s16
	global_load_lds_dwordx4 v196, s[98:99]
	s_add_u32 s98, s98, s0
	s_addc_u32 s99, s99, s1
	s_mov_b32 m0, s7
	s_nop 0
	global_load_lds_dwordx4 v192, s[98:99]
	s_add_i32 m0, s7, 0x2000
	s_nop 0
	global_load_lds_dwordx4 v196, s[98:99]
	s_add_u32 s98, s40, s14
	s_addc_u32 s99, s41, s15
	s_mov_b32 m0, s8
	s_nop 0
	global_load_lds_dwordx4 v190, s[98:99]
	s_mov_b32 m0, s70
	s_nop 0
	global_load_lds_dwordx4 v194, s[98:99]
	s_waitcnt vmcnt(8)
	s_waitcnt lgkmcnt(0)
	s_setprio 1
	s_barrier
	s_setprio 1
	s_waitcnt lgkmcnt(0)
	v_mfma_f32_16x16x32_bf16 v[82:85], v[42:45], v[66:69], v[94:97]
	v_mfma_f32_16x16x32_bf16 v[94:97], v[46:49], v[70:73], v[82:85]
	v_mfma_f32_16x16x32_bf16 v[82:85], v[58:61], v[66:69], v[90:93]
	v_mfma_f32_16x16x32_bf16 v[78:81], v[42:45], v[122:125], v[78:81]
	v_mfma_f32_16x16x32_bf16 v[74:77], v[58:61], v[122:125], v[74:77]
	v_mfma_f32_16x16x32_bf16 v[54:57], v[42:45], v[186:189], v[54:57]
	v_mfma_f32_16x16x32_bf16 v[50:53], v[58:61], v[186:189], v[50:53]
	v_mfma_f32_16x16x32_bf16 v[14:17], v[42:45], v[214:217], v[14:17]
	v_mfma_f32_16x16x32_bf16 v[10:13], v[58:61], v[214:217], v[10:13]
	v_mfma_f32_16x16x32_bf16 v[90:93], v[62:65], v[70:73], v[82:85]
	v_mfma_f32_16x16x32_bf16 v[78:81], v[46:49], v[134:137], v[78:81]
	v_mfma_f32_16x16x32_bf16 v[74:77], v[62:65], v[134:137], v[74:77]
	v_mfma_f32_16x16x32_bf16 v[54:57], v[46:49], v[210:213], v[54:57]
	v_mfma_f32_16x16x32_bf16 v[50:53], v[62:65], v[210:213], v[50:53]
	v_mfma_f32_16x16x32_bf16 v[14:17], v[46:49], v[218:221], v[14:17]
	v_mfma_f32_16x16x32_bf16 v[10:13], v[62:65], v[218:221], v[10:13]
	s_setprio 0
	s_setprio 1
	v_mfma_f32_16x16x32_bf16 v[18:21], v[146:149], v[66:69], v[18:21]
	v_mfma_f32_16x16x32_bf16 v[86:89], v[158:161], v[70:73], v[18:21]
	v_mfma_f32_16x16x32_bf16 v[18:21], v[170:173], v[66:69], v[22:25]
	v_mfma_f32_16x16x32_bf16 v[82:85], v[182:185], v[70:73], v[18:21]
	v_mfma_f32_16x16x32_bf16 v[18:21], v[146:149], v[122:125], v[26:29]
	v_mfma_f32_16x16x32_bf16 v[70:73], v[158:161], v[134:137], v[18:21]
	v_mfma_f32_16x16x32_bf16 v[18:21], v[170:173], v[122:125], v[30:33]
	v_mfma_f32_16x16x32_bf16 v[66:69], v[182:185], v[134:137], v[18:21]
	v_mfma_f32_16x16x32_bf16 v[18:21], v[146:149], v[186:189], v[38:41]
	v_mfma_f32_16x16x32_bf16 v[38:41], v[158:161], v[210:213], v[18:21]
	v_mfma_f32_16x16x32_bf16 v[18:21], v[170:173], v[186:189], v[34:37]
	v_mfma_f32_16x16x32_bf16 v[6:9], v[146:149], v[214:217], v[6:9]
	v_mfma_f32_16x16x32_bf16 v[2:5], v[170:173], v[214:217], v[2:5]
	v_mfma_f32_16x16x32_bf16 v[34:37], v[182:185], v[210:213], v[18:21]
	v_mfma_f32_16x16x32_bf16 v[6:9], v[158:161], v[218:221], v[6:9]
	v_mfma_f32_16x16x32_bf16 v[2:5], v[182:185], v[218:221], v[2:5]
	s_setprio 0
	s_barrier
	s_add_u32 s38, s38, 0x100
	s_addc_u32 s39, s39, 0
	s_add_u32 s42, s42, 0x100
	s_addc_u32 s43, s43, 0
	s_cmp_ge_i32 s44, s71
	s_mov_b32 s40, s44
	s_cbranch_scc0 .LBB0_1953

.LBB0_2027:
	v_mov_b32_e32 v235, 0x3b800000
	v_readlane_b32 s60, v254, 7
	s_or_b32 s0, s23, 8
	v_readlane_b32 s63, v254, 10
	v_readlane_b32 s62, v254, 9
	s_cmp_ge_i32 s0, s63
	v_readlane_b32 s61, v254, 8
	s_cbranch_scc0 .LBB0_2028
	s_getpc_b64 s[98:99]
